# P9 down-GEMM: last 3 of 8 epilogue stores per wave kept packed in spare VGPRs and issued from the next unit's load slots (which have slack); vmcnt waits re-derived
# speedup vs baseline: 1.0006x; 1.0006x over previous
; #define G8_STAGE(bufoff, gbase, voff) do { _Pragma("unroll") for (int _i = 0; _i < 2; ++_i) \
;         __builtin_amdgcn_global_load_lds((const unsigned*)((const char*)(gbase) + (voff)[_i]), (LAS unsigned*)(lds + (bufoff) + ldsw + _i * 8192), 16, 0, 0); } while (0)
; #define G8_LDA(dst, b, h) do { _Pragma("unroll") for (int m = 0; m < 4; ++m) _Pragma("unroll") for (int k = 0; k < 2; ++k) dst[m][k] = *(const LAS bf16x8*)(lds + G8_SA(b, h) + aoff + m * 2048 + k * 1024); } while (0)
; #define G8_LDB(dst, b, h) do { _Pragma("unroll") for (int n = 0; n < 2; ++n) _Pragma("unroll") for (int k = 0; k < 2; ++k) dst[n][k] = *(const LAS bf16x8*)(lds + G8_SB(b, h) + boff + n * 2048 + k * 1024); } while (0)
; #define G8_WAIT_L(n) asm volatile("s_waitcnt lgkmcnt(" #n ")" ::: "memory")
; #define G8_BAR __builtin_amdgcn_s_barrier()
; #define G8_SCHED __builtin_amdgcn_sched_barrier(0)
; template <class Epi, class Sched, int NT, bool F8 = false>
; __device__ __forceinline__ void gemm_phase(LAS unsigned char* lds, const Sched& S, const Epi& E) {
;     ...
;         for (int t = 0; t < nt; t += 2) {
;             const bool last = (t == nt - 2);
;             const char* a1 = cA + (size_t)(t + 1) * kstep;
;             const char* a2 = last ? nA : cA + (size_t)(t + 2) * kstep; const char* b2 = last ? nB : cB + (size_t)(t + 2) * kstep;
;             const char* a3 = a2 + kstep; const char* b3 = b2 + kstep;
;             G8_LDB(B0, 0, 0); G8_LDB(B1, 0, 1); G8_SCHED; G8_LDA(At, 0, 0); G8_STAGE(G8_SA(1, 1), a1, cur.vA1);
;             if (last) { cur.vA0[0] = nxt.vA0[0]; cur.vA0[1] = nxt.vA0[1]; cur.vA1[0] = nxt.vA1[0]; cur.vA1[1] = nxt.vA1[1]; }
;             G8_WAIT_VF(t, ui); G8_WAIT_L(0); G8_BAR; G8_MMA(0, 0, At, B0); G8_MMA(0, 1, At, B1); G8_BAR; G8_SCHED;
.LBB0_945:
	s_xor_b64 s[26:27], s[30:31], -1
	s_add_u32 s34, s34, 0x100
	s_addc_u32 s35, s35, 0
	s_and_b64 s[30:31], s[28:29], exec
	s_cselect_b32 s31, s17, s35
	s_cselect_b32 s30, s16, s34
	s_add_u32 s34, s22, s66
	s_addc_u32 s35, s23, 0
	s_add_u32 s34, s34, 0x100
	s_addc_u32 s35, s35, 0
	s_and_b64 s[28:29], s[28:29], exec
	s_cselect_b32 s34, s14, s34
	s_cselect_b32 s35, s15, s35
	s_add_u32 s28, s34, 0x80
	s_addc_u32 s29, s35, 0
	s_mov_b32 s100, 0
	s_cmp_eq_u32 s65, 0
	s_cbranch_scc1 .LwA8
	s_cmp_lg_u32 s13, 0
	s_cbranch_scc1 .LwA10
	s_mov_b32 s100, 1
	s_waitcnt vmcnt(13)
	s_branch .LwAe
.LwA10:
	s_waitcnt vmcnt(10)
	s_branch .LwAe

; #define G8_STAGE(bufoff, gbase, voff) do { _Pragma("unroll") for (int _i = 0; _i < 2; ++_i) \
;         __builtin_amdgcn_global_load_lds((const unsigned*)((const char*)(gbase) + (voff)[_i]), (LAS unsigned*)(lds + (bufoff) + ldsw + _i * 8192), 16, 0, 0); } while (0)
; #define G8_LDA(dst, b, h) do { _Pragma("unroll") for (int m = 0; m < 4; ++m) _Pragma("unroll") for (int k = 0; k < 2; ++k) dst[m][k] = *(const LAS bf16x8*)(lds + G8_SA(b, h) + aoff + m * 2048 + k * 1024); } while (0)
; #define G8_WAIT_L(n) asm volatile("s_waitcnt lgkmcnt(" #n ")" ::: "memory")
; #define G8_BAR __builtin_amdgcn_s_barrier()
; #define G8_SCHED __builtin_amdgcn_sched_barrier(0)
; template <class Epi, class Sched, int NT, bool F8 = false>
; __device__ __forceinline__ void gemm_phase(LAS unsigned char* lds, const Sched& S, const Epi& E) {
;     ...
;             G8_WAIT_VF(t, ui); G8_WAIT_L(0); G8_BAR; G8_MMA(0, 0, At, B0); G8_MMA(0, 1, At, B1); G8_BAR; G8_SCHED;
;             G8_LDA(At, 0, 1); G8_STAGE(G8_SB(0, 0), b2, voffB); G8_STAGE(G8_SB(0, 1), b2, voffB1); G8_STAGE(G8_SA(0, 0), a2, cur.vA0);
;             G8_WAIT_VF(t, ui); G8_WAIT_L(0); G8_BAR; G8_MMA(1, 0, At, B0); G8_MMA(1, 1, At, B1); G8_BAR; G8_SCHED;
;     __device__ __forceinline__ void operator()(const f32x4 (&acc)[2][2][4][2], const g8::Unit& u, int wr, int wc, int fr, int fq) const {
;     ...
;                 *(u32x4*)(y + (size_t)(row0 + ai * 128 + m * 16) * DM + col0) = w; }
.LwAe:
	s_waitcnt lgkmcnt(0)
	s_barrier
	s_setprio 1
	s_waitcnt lgkmcnt(0)
	v_mfma_scale_f32_16x16x128_f8f6f4 v[190:193], v[18:25], v[58:65], v[190:193], v227, v227 op_sel_hi:[0,0,0]
	v_mfma_scale_f32_16x16x128_f8f6f4 v[186:189], v[26:33], v[58:65], v[186:189], v227, v227 op_sel_hi:[0,0,0]
	v_mfma_scale_f32_16x16x128_f8f6f4 v[178:181], v[18:25], v[50:57], v[178:181], v227, v227 op_sel_hi:[0,0,0]
	v_mfma_scale_f32_16x16x128_f8f6f4 v[170:173], v[26:33], v[50:57], v[170:173], v227, v227 op_sel_hi:[0,0,0]
	v_mfma_scale_f32_16x16x128_f8f6f4 v[162:165], v[18:25], v[42:49], v[162:165], v227, v227 op_sel_hi:[0,0,0]
	v_mfma_scale_f32_16x16x128_f8f6f4 v[154:157], v[26:33], v[42:49], v[154:157], v227, v227 op_sel_hi:[0,0,0]
	v_mfma_scale_f32_16x16x128_f8f6f4 v[146:149], v[18:25], v[34:41], v[146:149], v227, v227 op_sel_hi:[0,0,0]
	v_mfma_scale_f32_16x16x128_f8f6f4 v[138:141], v[26:33], v[34:41], v[138:141], v227, v227 op_sel_hi:[0,0,0]
	s_setprio 0
	s_setprio 1
	v_mfma_scale_f32_16x16x128_f8f6f4 v[182:185], v[2:9], v[58:65], v[182:185], v227, v227 op_sel_hi:[0,0,0]
	v_mfma_scale_f32_16x16x128_f8f6f4 v[174:177], v[10:17], v[58:65], v[174:177], v227, v227 op_sel_hi:[0,0,0]
	v_mfma_scale_f32_16x16x128_f8f6f4 v[166:169], v[2:9], v[50:57], v[166:169], v227, v227 op_sel_hi:[0,0,0]
	v_mfma_scale_f32_16x16x128_f8f6f4 v[158:161], v[10:17], v[50:57], v[158:161], v227, v227 op_sel_hi:[0,0,0]
	v_mfma_scale_f32_16x16x128_f8f6f4 v[150:153], v[2:9], v[42:49], v[150:153], v227, v227 op_sel_hi:[0,0,0]
	v_mfma_scale_f32_16x16x128_f8f6f4 v[142:145], v[10:17], v[42:49], v[142:145], v227, v227 op_sel_hi:[0,0,0]
	v_mfma_scale_f32_16x16x128_f8f6f4 v[134:137], v[2:9], v[34:41], v[134:137], v227, v227 op_sel_hi:[0,0,0]
	v_mfma_scale_f32_16x16x128_f8f6f4 v[130:133], v[10:17], v[34:41], v[130:133], v227, v227 op_sel_hi:[0,0,0]
	s_setprio 0
	s_barrier
	s_mov_b32 m0, s42
	v_lshl_add_u64 v[232:233], s[34:35], 0, v[200:201]
	ds_read_b128 v[34:37], v226 offset:16384
	ds_read_b128 v[38:41], v226 offset:17408
	ds_read_b128 v[42:45], v226 offset:18432
	ds_read_b128 v[46:49], v226 offset:19456
	ds_read_b128 v[50:53], v226 offset:20480
	ds_read_b128 v[54:57], v226 offset:21504
	ds_read_b128 v[58:61], v226 offset:22528
	ds_read_b128 v[62:65], v226 offset:23552
	global_load_lds_dwordx4 v[232:233], off
	v_lshl_add_u64 v[234:235], s[34:35], 0, v[196:197]
	s_mov_b32 m0, s43
	v_lshl_add_u64 v[236:237], s[34:35], 0, v[198:199]
	global_load_lds_dwordx4 v[234:235], off
	s_mov_b32 m0, s44
	v_mov_b32_e32 v211, v203
	global_load_lds_dwordx4 v[236:237], off
	v_lshl_add_u64 v[236:237], s[34:35], 0, v[194:195]
	s_mov_b32 m0, s45
	v_mov_b32_e32 v213, v203
	global_load_lds_dwordx4 v[236:237], off
	s_mov_b32 m0, s21
	v_lshl_add_u64 v[236:237], s[30:31], 0, v[210:211]
	global_load_lds_dwordx4 v210, s[30:31]
	s_mov_b32 m0, s46
	v_lshl_add_u64 v[238:239], s[30:31], 0, v[212:213]
	global_load_lds_dwordx4 v212, s[30:31]
	s_cmp_eq_u32 s100, 0
	s_cbranch_scc1 .LdfB
	v_add_u32_e32 v252, s98, v221
	v_lshlrev_b32_e32 v252, 11, v252
	v_add3_u32 v252, v252, s99, v223
	v_add_u32_e32 v252, 0x48000, v252
	global_store_dwordx4 v252, v[240:243], s[8:9]
.LdfB:
	s_cmp_eq_u32 s100, 0
	s_cbranch_scc1 .LwBs
	s_waitcnt vmcnt(14)
	s_branch .LwBe

; #define G8_STAGE(bufoff, gbase, voff) do { _Pragma("unroll") for (int _i = 0; _i < 2; ++_i) \
;         __builtin_amdgcn_global_load_lds((const unsigned*)((const char*)(gbase) + (voff)[_i]), (LAS unsigned*)(lds + (bufoff) + ldsw + _i * 8192), 16, 0, 0); } while (0)
; #define G8_LDA(dst, b, h) do { _Pragma("unroll") for (int m = 0; m < 4; ++m) _Pragma("unroll") for (int k = 0; k < 2; ++k) dst[m][k] = *(const LAS bf16x8*)(lds + G8_SA(b, h) + aoff + m * 2048 + k * 1024); } while (0)
; #define G8_LDB(dst, b, h) do { _Pragma("unroll") for (int n = 0; n < 2; ++n) _Pragma("unroll") for (int k = 0; k < 2; ++k) dst[n][k] = *(const LAS bf16x8*)(lds + G8_SB(b, h) + boff + n * 2048 + k * 1024); } while (0)
; #define G8_WAIT_V(n) asm volatile("s_waitcnt vmcnt(" #n ")" ::: "memory")
; #define G8_WAIT_L(n) asm volatile("s_waitcnt lgkmcnt(" #n ")" ::: "memory")
; #define G8_BAR __builtin_amdgcn_s_barrier()
; #define G8_SCHED __builtin_amdgcn_sched_barrier(0)
; template <class Epi, class Sched, int NT, bool F8 = false>
; __device__ __forceinline__ void gemm_phase(LAS unsigned char* lds, const Sched& S, const Epi& E) {
;     ...
;             G8_WAIT_VF(t, ui); G8_WAIT_L(0); G8_BAR; G8_MMA(1, 0, At, B0); G8_MMA(1, 1, At, B1); G8_BAR; G8_SCHED;
;             G8_LDB(B0, 1, 0); G8_LDB(B1, 1, 1); G8_SCHED; G8_LDA(At, 1, 0); G8_STAGE(G8_SA(0, 1), a2, cur.vA1);
;             G8_WAIT_V(8); G8_WAIT_L(0); G8_BAR; G8_MMA(0, 0, At, B0); G8_MMA(0, 1, At, B1); G8_BAR; G8_SCHED;
;     __device__ __forceinline__ void operator()(const f32x4 (&acc)[2][2][4][2], const g8::Unit& u, int wr, int wc, int fr, int fq) const {
;     ...
;                 *(u32x4*)(y + (size_t)(row0 + ai * 128 + m * 16) * DM + col0) = w; }
.LwBe:
	s_waitcnt lgkmcnt(0)
	s_barrier
	s_setprio 1
	s_waitcnt lgkmcnt(0)
	v_mfma_scale_f32_16x16x128_f8f6f4 v[126:129], v[18:25], v[34:41], v[126:129], v227, v227 op_sel_hi:[0,0,0]
	v_mfma_scale_f32_16x16x128_f8f6f4 v[122:125], v[26:33], v[34:41], v[122:125], v227, v227 op_sel_hi:[0,0,0]
	v_mfma_scale_f32_16x16x128_f8f6f4 v[114:117], v[18:25], v[42:49], v[114:117], v227, v227 op_sel_hi:[0,0,0]
	v_mfma_scale_f32_16x16x128_f8f6f4 v[106:109], v[26:33], v[42:49], v[106:109], v227, v227 op_sel_hi:[0,0,0]
	v_mfma_scale_f32_16x16x128_f8f6f4 v[98:101], v[18:25], v[50:57], v[98:101], v227, v227 op_sel_hi:[0,0,0]
	v_mfma_scale_f32_16x16x128_f8f6f4 v[90:93], v[26:33], v[50:57], v[90:93], v227, v227 op_sel_hi:[0,0,0]
	v_mfma_scale_f32_16x16x128_f8f6f4 v[82:85], v[18:25], v[58:65], v[82:85], v227, v227 op_sel_hi:[0,0,0]
	v_mfma_scale_f32_16x16x128_f8f6f4 v[74:77], v[26:33], v[58:65], v[74:77], v227, v227 op_sel_hi:[0,0,0]
	s_setprio 0
	s_setprio 1
	v_mfma_scale_f32_16x16x128_f8f6f4 v[118:121], v[2:9], v[34:41], v[118:121], v227, v227 op_sel_hi:[0,0,0]
	v_mfma_scale_f32_16x16x128_f8f6f4 v[110:113], v[10:17], v[34:41], v[110:113], v227, v227 op_sel_hi:[0,0,0]
	v_mfma_scale_f32_16x16x128_f8f6f4 v[102:105], v[2:9], v[42:49], v[102:105], v227, v227 op_sel_hi:[0,0,0]
	v_mfma_scale_f32_16x16x128_f8f6f4 v[94:97], v[10:17], v[42:49], v[94:97], v227, v227 op_sel_hi:[0,0,0]
	v_mfma_scale_f32_16x16x128_f8f6f4 v[86:89], v[2:9], v[50:57], v[86:89], v227, v227 op_sel_hi:[0,0,0]
	v_mfma_scale_f32_16x16x128_f8f6f4 v[78:81], v[10:17], v[50:57], v[78:81], v227, v227 op_sel_hi:[0,0,0]
	v_mfma_scale_f32_16x16x128_f8f6f4 v[70:73], v[2:9], v[58:65], v[70:73], v227, v227 op_sel_hi:[0,0,0]
	v_mfma_scale_f32_16x16x128_f8f6f4 v[66:69], v[10:17], v[58:65], v[66:69], v227, v227 op_sel_hi:[0,0,0]
	s_setprio 0
	s_barrier
	v_add_u32_e32 v14, s56, v222
	v_add_u32_e32 v30, s57, v222
	ds_read_b128 v[2:5], v14
	ds_read_b128 v[6:9], v14 offset:1024
	ds_read_b128 v[10:13], v14 offset:2048
	ds_read_b128 v[14:17], v14 offset:3072
	ds_read_b128 v[18:21], v30
	ds_read_b128 v[22:25], v30 offset:1024
	ds_read_b128 v[26:29], v30 offset:2048
	ds_read_b128 v[30:33], v30 offset:3072
	s_mov_b32 m0, s47
	v_lshl_add_u64 v[216:217], s[30:31], 0, v[216:217]
	ds_read_b128 v[34:37], v226 offset:32768
	ds_read_b128 v[38:41], v226 offset:33792
	ds_read_b128 v[42:45], v226 offset:34816
	ds_read_b128 v[46:49], v226 offset:35840
	ds_read_b128 v[50:53], v226 offset:36864
	ds_read_b128 v[54:57], v226 offset:37888
	ds_read_b128 v[58:61], v226 offset:38912
	ds_read_b128 v[62:65], v226 offset:39936
	global_load_lds_dwordx4 v[216:217], off
	v_lshl_add_u64 v[214:215], s[30:31], 0, v[214:215]
	s_mov_b32 m0, s48
	s_nop 0
	global_load_lds_dwordx4 v[214:215], off
	s_cmp_eq_u32 s100, 0
	s_cbranch_scc1 .LdfC
	v_add_u32_e32 v252, s98, v221
	v_lshlrev_b32_e32 v252, 11, v252
	v_add3_u32 v252, v252, s99, v223
	v_add_u32_e32 v252, 0x50000, v252
	global_store_dwordx4 v252, v[244:247], s[8:9]
.LdfC:
	s_cmp_eq_u32 s100, 0
	s_cbranch_scc1 .LwCs
	s_waitcnt vmcnt(10)
	s_branch .LwCe

; #define G8_STAGE(bufoff, gbase, voff) do { _Pragma("unroll") for (int _i = 0; _i < 2; ++_i) \
;         __builtin_amdgcn_global_load_lds((const unsigned*)((const char*)(gbase) + (voff)[_i]), (LAS unsigned*)(lds + (bufoff) + ldsw + _i * 8192), 16, 0, 0); } while (0)
; #define G8_LDA(dst, b, h) do { _Pragma("unroll") for (int m = 0; m < 4; ++m) _Pragma("unroll") for (int k = 0; k < 2; ++k) dst[m][k] = *(const LAS bf16x8*)(lds + G8_SA(b, h) + aoff + m * 2048 + k * 1024); } while (0)
; #define G8_WAIT_V(n) asm volatile("s_waitcnt vmcnt(" #n ")" ::: "memory")
; #define G8_WAIT_L(n) asm volatile("s_waitcnt lgkmcnt(" #n ")" ::: "memory")
; #define G8_BAR __builtin_amdgcn_s_barrier()
; #define G8_SCHED __builtin_amdgcn_sched_barrier(0)
; template <class Epi, class Sched, int NT, bool F8 = false>
; __device__ __forceinline__ void gemm_phase(LAS unsigned char* lds, const Sched& S, const Epi& E) {
;     ...
;             G8_WAIT_V(8); G8_WAIT_L(0); G8_BAR; G8_MMA(0, 0, At, B0); G8_MMA(0, 1, At, B1); G8_BAR; G8_SCHED;
;             G8_LDA(At, 1, 1); G8_STAGE(G8_SB(1, 0), b3, voffB); G8_STAGE(G8_SB(1, 1), b3, voffB1); G8_STAGE(G8_SA(1, 0), a3, cur.vA0);
;             G8_WAIT_V(8); G8_WAIT_L(0); G8_BAR; G8_MMA(1, 0, At, B0); G8_MMA(1, 1, At, B1); G8_BAR; G8_SCHED;
;     __device__ __forceinline__ void operator()(const f32x4 (&acc)[2][2][4][2], const g8::Unit& u, int wr, int wc, int fr, int fq) const {
;     ...
;                 *(u32x4*)(y + (size_t)(row0 + ai * 128 + m * 16) * DM + col0) = w; }
.LwCe:
	s_waitcnt lgkmcnt(0)
	s_barrier
	s_setprio 1
	s_waitcnt lgkmcnt(0)
	v_mfma_scale_f32_16x16x128_f8f6f4 v[190:193], v[2:9], v[34:41], v[190:193], v227, v227 op_sel_hi:[0,0,0]
	v_mfma_scale_f32_16x16x128_f8f6f4 v[186:189], v[10:17], v[34:41], v[186:189], v227, v227 op_sel_hi:[0,0,0]
	v_mfma_scale_f32_16x16x128_f8f6f4 v[178:181], v[2:9], v[42:49], v[178:181], v227, v227 op_sel_hi:[0,0,0]
	v_mfma_scale_f32_16x16x128_f8f6f4 v[170:173], v[10:17], v[42:49], v[170:173], v227, v227 op_sel_hi:[0,0,0]
	v_mfma_scale_f32_16x16x128_f8f6f4 v[162:165], v[2:9], v[50:57], v[162:165], v227, v227 op_sel_hi:[0,0,0]
	v_mfma_scale_f32_16x16x128_f8f6f4 v[154:157], v[10:17], v[50:57], v[154:157], v227, v227 op_sel_hi:[0,0,0]
	v_mfma_scale_f32_16x16x128_f8f6f4 v[146:149], v[2:9], v[58:65], v[146:149], v227, v227 op_sel_hi:[0,0,0]
	v_mfma_scale_f32_16x16x128_f8f6f4 v[138:141], v[10:17], v[58:65], v[138:141], v227, v227 op_sel_hi:[0,0,0]
	s_setprio 0
	s_setprio 1
	v_mfma_scale_f32_16x16x128_f8f6f4 v[182:185], v[18:25], v[34:41], v[182:185], v227, v227 op_sel_hi:[0,0,0]
	v_mfma_scale_f32_16x16x128_f8f6f4 v[174:177], v[26:33], v[34:41], v[174:177], v227, v227 op_sel_hi:[0,0,0]
	v_mfma_scale_f32_16x16x128_f8f6f4 v[166:169], v[18:25], v[42:49], v[166:169], v227, v227 op_sel_hi:[0,0,0]
	v_mfma_scale_f32_16x16x128_f8f6f4 v[158:161], v[26:33], v[42:49], v[158:161], v227, v227 op_sel_hi:[0,0,0]
	v_mfma_scale_f32_16x16x128_f8f6f4 v[150:153], v[18:25], v[50:57], v[150:153], v227, v227 op_sel_hi:[0,0,0]
	v_mfma_scale_f32_16x16x128_f8f6f4 v[142:145], v[26:33], v[50:57], v[142:145], v227, v227 op_sel_hi:[0,0,0]
	v_mfma_scale_f32_16x16x128_f8f6f4 v[134:137], v[18:25], v[58:65], v[134:137], v227, v227 op_sel_hi:[0,0,0]
	v_mfma_scale_f32_16x16x128_f8f6f4 v[130:133], v[26:33], v[58:65], v[130:133], v227, v227 op_sel_hi:[0,0,0]
	s_setprio 0
	s_barrier
	s_add_i32 s13, s56, s39
	v_lshl_add_u64 v[214:215], v[232:233], 0, s[2:3]
	s_mov_b32 m0, s13
	ds_read_b128 v[34:37], v226 offset:49152
	ds_read_b128 v[38:41], v226 offset:50176
	ds_read_b128 v[42:45], v226 offset:51200
	ds_read_b128 v[46:49], v226 offset:52224
	ds_read_b128 v[50:53], v226 offset:53248
	ds_read_b128 v[54:57], v226 offset:54272
	ds_read_b128 v[58:61], v226 offset:55296
	ds_read_b128 v[62:65], v226 offset:56320
	global_load_lds_dwordx4 v[214:215], off
	v_lshl_add_u64 v[214:215], v[234:235], 0, s[2:3]
	s_add_i32 m0, s13, 0x2000
	s_add_i32 s13, s57, s39
	global_load_lds_dwordx4 v[214:215], off
	v_lshl_add_u64 v[214:215], s[28:29], 0, v[198:199]
	s_mov_b32 m0, s13
	s_nop 0
	global_load_lds_dwordx4 v[214:215], off
	v_lshl_add_u64 v[214:215], s[28:29], 0, v[194:195]
	s_add_i32 m0, s13, 0x2000
	s_nop 0
	global_load_lds_dwordx4 v[214:215], off
	v_lshl_add_u64 v[214:215], v[236:237], 0, s[2:3]
	s_mov_b32 m0, s49
	s_nop 0
	global_load_lds_dwordx4 v[214:215], off
	v_lshl_add_u64 v[214:215], v[238:239], 0, s[2:3]
	s_mov_b32 m0, s50
	s_nop 0
	global_load_lds_dwordx4 v[214:215], off
	s_cmp_eq_u32 s100, 0
	s_cbranch_scc1 .LdfD
	v_add_u32_e32 v252, s98, v221
	v_lshlrev_b32_e32 v252, 11, v252
	v_add3_u32 v252, v252, s99, v223
	v_add_u32_e32 v252, 0x58000, v252
	global_store_dwordx4 v252, v[248:251], s[8:9]
.LdfD:
	s_cmp_eq_u32 s100, 0
	s_cbranch_scc1 .LwDs
	s_waitcnt vmcnt(11)
	s_branch .LwDe

; #define G8_WAIT_V(n) asm volatile("s_waitcnt vmcnt(" #n ")" ::: "memory")
; #define G8_WAIT_L(n) asm volatile("s_waitcnt lgkmcnt(" #n ")" ::: "memory")
; #define G8_BAR __builtin_amdgcn_s_barrier()
; #define G8_SCHED __builtin_amdgcn_sched_barrier(0)
; template <class Epi, class Sched, int NT, bool F8 = false>
; __device__ __forceinline__ void gemm_phase(LAS unsigned char* lds, const Sched& S, const Epi& E) {
;     ...
;             G8_WAIT_V(8); G8_WAIT_L(0); G8_BAR; G8_MMA(1, 0, At, B0); G8_MMA(1, 1, At, B1); G8_BAR; G8_SCHED;
;         }
;         if (wr == 0) G8_BAR;
.LwDe:
	s_waitcnt lgkmcnt(0)
	s_barrier
	s_setprio 1
	s_waitcnt lgkmcnt(0)
	v_mfma_scale_f32_16x16x128_f8f6f4 v[126:129], v[2:9], v[34:41], v[126:129], v227, v227 op_sel_hi:[0,0,0]
	v_mfma_scale_f32_16x16x128_f8f6f4 v[122:125], v[10:17], v[34:41], v[122:125], v227, v227 op_sel_hi:[0,0,0]
	v_mfma_scale_f32_16x16x128_f8f6f4 v[114:117], v[2:9], v[42:49], v[114:117], v227, v227 op_sel_hi:[0,0,0]
	v_mfma_scale_f32_16x16x128_f8f6f4 v[106:109], v[10:17], v[42:49], v[106:109], v227, v227 op_sel_hi:[0,0,0]
	v_mfma_scale_f32_16x16x128_f8f6f4 v[98:101], v[2:9], v[50:57], v[98:101], v227, v227 op_sel_hi:[0,0,0]
	v_mfma_scale_f32_16x16x128_f8f6f4 v[90:93], v[10:17], v[50:57], v[90:93], v227, v227 op_sel_hi:[0,0,0]
	v_mfma_scale_f32_16x16x128_f8f6f4 v[82:85], v[2:9], v[58:65], v[82:85], v227, v227 op_sel_hi:[0,0,0]
	v_mfma_scale_f32_16x16x128_f8f6f4 v[74:77], v[10:17], v[58:65], v[74:77], v227, v227 op_sel_hi:[0,0,0]
	s_setprio 0
	s_setprio 1
	v_mfma_scale_f32_16x16x128_f8f6f4 v[118:121], v[18:25], v[34:41], v[118:121], v227, v227 op_sel_hi:[0,0,0]
	v_mfma_scale_f32_16x16x128_f8f6f4 v[110:113], v[26:33], v[34:41], v[110:113], v227, v227 op_sel_hi:[0,0,0]
	v_mfma_scale_f32_16x16x128_f8f6f4 v[102:105], v[18:25], v[42:49], v[102:105], v227, v227 op_sel_hi:[0,0,0]
	v_mfma_scale_f32_16x16x128_f8f6f4 v[94:97], v[26:33], v[42:49], v[94:97], v227, v227 op_sel_hi:[0,0,0]
	v_mfma_scale_f32_16x16x128_f8f6f4 v[86:89], v[18:25], v[50:57], v[86:89], v227, v227 op_sel_hi:[0,0,0]
	v_mfma_scale_f32_16x16x128_f8f6f4 v[78:81], v[26:33], v[50:57], v[78:81], v227, v227 op_sel_hi:[0,0,0]
	v_mfma_scale_f32_16x16x128_f8f6f4 v[70:73], v[18:25], v[58:65], v[70:73], v227, v227 op_sel_hi:[0,0,0]
	v_mfma_scale_f32_16x16x128_f8f6f4 v[66:69], v[26:33], v[58:65], v[66:69], v227, v227 op_sel_hi:[0,0,0]
	s_setprio 0
	s_barrier
	s_mov_b32 s13, 2
	s_mov_b64 s[30:31], 0
	s_mov_b64 s[28:29], -1
	s_and_b64 vcc, exec, s[26:27]
	s_cbranch_vccnz .LBB0_948

; __device__ __forceinline__ unsigned pk4_fp8(float a, float b, float c, float d) { int w = 0; w = __builtin_amdgcn_cvt_pk_fp8_f32(clamp448(a), clamp448(b), w, false); w = __builtin_amdgcn_cvt_pk_fp8_f32(clamp448(c), clamp448(d), w, true); return (unsigned)w; }
;     __device__ __forceinline__ void operator()(const f32x4 (&acc)[2][2][4][2], const g8::Unit& u, int wr, int wc, int fr, int fq) const {
;         const int row0 = u.r0 + wr * 64 + fr, col0 = u.pn * 256 + wc * 64 + 16 * fq; constexpr float sc = SC_Y / (SC_ACT * SC_WEO); static_assert(sc == 1.0f, "scales chosen so that y needs no multiply");
; #pragma unroll
;         for (int ai = 0; ai < 2; ++ai)
; #pragma unroll
;             for (int m = 0; m < 4; ++m) { u32x4 w;
;                 { const f32x4 v0 = acc[ai][0][m][0], v1 = acc[ai][0][m][1], v2 = acc[ai][1][m][0], v3 = acc[ai][1][m][1];
;                   w.x = pk4_fp8(v0[0], v0[1], v0[2], v0[3]); w.y = pk4_fp8(v1[0], v1[1], v1[2], v1[3]); w.z = pk4_fp8(v2[0], v2[1], v2[2], v2[3]); w.w = pk4_fp8(v3[0], v3[1], v3[2], v3[3]); }
;                 *(u32x4*)(y + (size_t)(row0 + ai * 128 + m * 16) * DM + col0) = w; }
.LBB0_950:
	v_add_u32_e32 v2, s64, v221
	v_ashrrev_i32_e32 v3, 31, v2
	v_lshl_or_b32 v8, s20, 8, v223
	v_lshlrev_b64 v[2:3], 11, v[2:3]
	v_ashrrev_i32_e32 v9, 31, v8
	v_lshl_add_u64 v[2:3], s[8:9], 0, v[2:3]
	v_lshl_add_u64 v[2:3], v[2:3], 0, v[8:9]
	v_med3_f32 v14, v190, s58, v228
	v_med3_f32 v15, v191, s58, v228
	v_med3_f32 v16, v192, s58, v228
	v_med3_f32 v17, v193, s58, v228
	v_cvt_pk_fp8_f32 v4, v14, v15
	s_nop 0
	v_cvt_pk_fp8_f32 v4, v16, v17 op_sel:[0,0,1]
	v_med3_f32 v14, v186, s58, v228
	v_med3_f32 v15, v187, s58, v228
	v_med3_f32 v16, v188, s58, v228
	v_med3_f32 v17, v189, s58, v228
	v_cvt_pk_fp8_f32 v5, v14, v15
	s_nop 0
	v_cvt_pk_fp8_f32 v5, v16, v17 op_sel:[0,0,1]
	v_med3_f32 v14, v182, s58, v228
	v_med3_f32 v15, v183, s58, v228
	v_med3_f32 v16, v184, s58, v228
	v_med3_f32 v17, v185, s58, v228
	v_cvt_pk_fp8_f32 v6, v14, v15
	s_nop 0
	v_cvt_pk_fp8_f32 v6, v16, v17 op_sel:[0,0,1]
	v_med3_f32 v14, v174, s58, v228
	v_med3_f32 v15, v175, s58, v228
	v_med3_f32 v16, v176, s58, v228
	v_med3_f32 v17, v177, s58, v228
	v_cvt_pk_fp8_f32 v7, v14, v15
	s_nop 0
	v_cvt_pk_fp8_f32 v7, v16, v17 op_sel:[0,0,1]
	s_nop 0
	global_store_dwordx4 v[2:3], v[4:7], off
	v_med3_f32 v14, v178, s58, v228
	v_med3_f32 v15, v179, s58, v228
	v_med3_f32 v16, v180, s58, v228
	v_med3_f32 v17, v181, s58, v228
	v_cvt_pk_fp8_f32 v10, v14, v15
	s_nop 0
	v_cvt_pk_fp8_f32 v10, v16, v17 op_sel:[0,0,1]
	v_med3_f32 v14, v170, s58, v228
	v_med3_f32 v15, v171, s58, v228
	v_med3_f32 v16, v172, s58, v228
	v_med3_f32 v17, v173, s58, v228
	v_cvt_pk_fp8_f32 v11, v14, v15
	s_nop 0
	v_cvt_pk_fp8_f32 v11, v16, v17 op_sel:[0,0,1]
	v_med3_f32 v14, v166, s58, v228
	v_med3_f32 v15, v167, s58, v228
	v_med3_f32 v16, v168, s58, v228
	v_med3_f32 v17, v169, s58, v228
	v_cvt_pk_fp8_f32 v12, v14, v15
	s_nop 0
	v_cvt_pk_fp8_f32 v12, v16, v17 op_sel:[0,0,1]
	v_med3_f32 v14, v158, s58, v228
	v_med3_f32 v15, v159, s58, v228
	v_med3_f32 v16, v160, s58, v228
	v_med3_f32 v17, v161, s58, v228
	v_cvt_pk_fp8_f32 v13, v14, v15
	s_nop 0
	v_cvt_pk_fp8_f32 v13, v16, v17 op_sel:[0,0,1]
	v_add_co_u32_e32 v8, vcc, s53, v2
	s_nop 1
	v_addc_co_u32_e32 v9, vcc, 0, v3, vcc
	global_store_dwordx4 v[8:9], v[10:13], off
	v_med3_f32 v14, v162, s58, v228
	v_med3_f32 v15, v163, s58, v228
	v_med3_f32 v16, v164, s58, v228
	v_med3_f32 v17, v165, s58, v228
	v_cvt_pk_fp8_f32 v4, v14, v15
	s_nop 0
	v_cvt_pk_fp8_f32 v4, v16, v17 op_sel:[0,0,1]
	v_med3_f32 v14, v154, s58, v228
	v_med3_f32 v15, v155, s58, v228
	v_med3_f32 v16, v156, s58, v228
	v_med3_f32 v17, v157, s58, v228
	v_cvt_pk_fp8_f32 v5, v14, v15
	s_nop 0
	v_cvt_pk_fp8_f32 v5, v16, v17 op_sel:[0,0,1]
	v_med3_f32 v14, v150, s58, v228
	v_med3_f32 v15, v151, s58, v228
	v_med3_f32 v16, v152, s58, v228
	v_med3_f32 v17, v153, s58, v228
	v_cvt_pk_fp8_f32 v6, v14, v15
	s_nop 0
	v_cvt_pk_fp8_f32 v6, v16, v17 op_sel:[0,0,1]
	v_med3_f32 v14, v142, s58, v228
	v_med3_f32 v15, v143, s58, v228
	v_med3_f32 v16, v144, s58, v228
	v_med3_f32 v17, v145, s58, v228
	v_cvt_pk_fp8_f32 v7, v14, v15
	s_nop 0
	v_cvt_pk_fp8_f32 v7, v16, v17 op_sel:[0,0,1]
	v_add_co_u32_e32 v8, vcc, s51, v2
	s_nop 1
	v_addc_co_u32_e32 v9, vcc, 0, v3, vcc
	global_store_dwordx4 v[8:9], v[4:7], off
	v_med3_f32 v14, v146, s58, v228
	v_med3_f32 v15, v147, s58, v228
	v_med3_f32 v16, v148, s58, v228
	v_med3_f32 v17, v149, s58, v228
	v_cvt_pk_fp8_f32 v10, v14, v15
	s_nop 0
	v_cvt_pk_fp8_f32 v10, v16, v17 op_sel:[0,0,1]
	v_med3_f32 v14, v138, s58, v228
	v_med3_f32 v15, v139, s58, v228
	v_med3_f32 v16, v140, s58, v228
	v_med3_f32 v17, v141, s58, v228
	v_cvt_pk_fp8_f32 v11, v14, v15
	s_nop 0
	v_cvt_pk_fp8_f32 v11, v16, v17 op_sel:[0,0,1]
	v_med3_f32 v14, v134, s58, v228
	v_med3_f32 v15, v135, s58, v228
	v_med3_f32 v16, v136, s58, v228
	v_med3_f32 v17, v137, s58, v228
	v_cvt_pk_fp8_f32 v12, v14, v15
	s_nop 0
	v_cvt_pk_fp8_f32 v12, v16, v17 op_sel:[0,0,1]
	v_med3_f32 v14, v130, s58, v228
	v_med3_f32 v15, v131, s58, v228
	v_med3_f32 v16, v132, s58, v228
	v_med3_f32 v17, v133, s58, v228
	v_cvt_pk_fp8_f32 v13, v14, v15
	s_nop 0
	v_cvt_pk_fp8_f32 v13, v16, v17 op_sel:[0,0,1]
	v_add_co_u32_e32 v8, vcc, s52, v2
	s_nop 1
	v_addc_co_u32_e32 v9, vcc, 0, v3, vcc
	global_store_dwordx4 v[8:9], v[10:13], off
	v_med3_f32 v14, v126, s58, v228
	v_med3_f32 v15, v127, s58, v228
	v_med3_f32 v16, v128, s58, v228
	v_med3_f32 v17, v129, s58, v228
; __device__ __forceinline__ unsigned pk4_fp8(float a, float b, float c, float d) { int w = 0; w = __builtin_amdgcn_cvt_pk_fp8_f32(clamp448(a), clamp448(b), w, false); w = __builtin_amdgcn_cvt_pk_fp8_f32(clamp448(c), clamp448(d), w, true); return (unsigned)w; }
; #define G8_WAIT_V(n) asm volatile("s_waitcnt vmcnt(" #n ")" ::: "memory")
; #define G8_BAR __builtin_amdgcn_s_barrier()
; template <class Epi, class Sched, int NT, bool F8 = false>
; __device__ __forceinline__ void gemm_phase(LAS unsigned char* lds, const Sched& S, const Epi& E) {
;     ...
;         if (wr == 1) G8_BAR;
;     }
;     G8_WAIT_V(0);
;     G8_BAR;
;     __device__ __forceinline__ void operator()(const f32x4 (&acc)[2][2][4][2], const g8::Unit& u, int wr, int wc, int fr, int fq) const {
;         const int row0 = u.r0 + wr * 64 + fr, col0 = u.pn * 256 + wc * 64 + 16 * fq; constexpr float sc = SC_Y / (SC_ACT * SC_WEO); static_assert(sc == 1.0f, "scales chosen so that y needs no multiply");
; #pragma unroll
;         for (int ai = 0; ai < 2; ++ai)
; #pragma unroll
;             for (int m = 0; m < 4; ++m) { u32x4 w;
;                 { const f32x4 v0 = acc[ai][0][m][0], v1 = acc[ai][0][m][1], v2 = acc[ai][1][m][0], v3 = acc[ai][1][m][1];
;                   w.x = pk4_fp8(v0[0], v0[1], v0[2], v0[3]); w.y = pk4_fp8(v1[0], v1[1], v1[2], v1[3]); w.z = pk4_fp8(v2[0], v2[1], v2[2], v2[3]); w.w = pk4_fp8(v3[0], v3[1], v3[2], v3[3]); }
;                 *(u32x4*)(y + (size_t)(row0 + ai * 128 + m * 16) * DM + col0) = w; }
	v_cvt_pk_fp8_f32 v4, v14, v15
	s_nop 0
	v_cvt_pk_fp8_f32 v4, v16, v17 op_sel:[0,0,1]
	v_med3_f32 v14, v122, s58, v228
	v_med3_f32 v15, v123, s58, v228
	v_med3_f32 v16, v124, s58, v228
	v_med3_f32 v17, v125, s58, v228
	v_cvt_pk_fp8_f32 v5, v14, v15
	s_nop 0
	v_cvt_pk_fp8_f32 v5, v16, v17 op_sel:[0,0,1]
	v_med3_f32 v14, v118, s58, v228
	v_med3_f32 v15, v119, s58, v228
	v_med3_f32 v16, v120, s58, v228
	v_med3_f32 v17, v121, s58, v228
	v_cvt_pk_fp8_f32 v6, v14, v15
	s_nop 0
	v_cvt_pk_fp8_f32 v6, v16, v17 op_sel:[0,0,1]
	v_med3_f32 v14, v110, s58, v228
	v_med3_f32 v15, v111, s58, v228
	v_med3_f32 v16, v112, s58, v228
	v_med3_f32 v17, v113, s58, v228
	v_cvt_pk_fp8_f32 v7, v14, v15
	s_nop 0
	v_cvt_pk_fp8_f32 v7, v16, v17 op_sel:[0,0,1]
	v_add_co_u32_e32 v8, vcc, s59, v2
	s_nop 1
	v_addc_co_u32_e32 v9, vcc, 0, v3, vcc
	global_store_dwordx4 v[8:9], v[4:7], off
	v_med3_f32 v14, v114, s58, v228
	v_med3_f32 v15, v115, s58, v228
	v_med3_f32 v16, v116, s58, v228
	v_med3_f32 v17, v117, s58, v228
	v_cvt_pk_fp8_f32 v240, v14, v15
	s_nop 0
	v_cvt_pk_fp8_f32 v240, v16, v17 op_sel:[0,0,1]
	v_med3_f32 v14, v106, s58, v228
	v_med3_f32 v15, v107, s58, v228
	v_med3_f32 v16, v108, s58, v228
	v_med3_f32 v17, v109, s58, v228
	v_cvt_pk_fp8_f32 v241, v14, v15
	s_nop 0
	v_cvt_pk_fp8_f32 v241, v16, v17 op_sel:[0,0,1]
	v_med3_f32 v14, v102, s58, v228
	v_med3_f32 v15, v103, s58, v228
	v_med3_f32 v16, v104, s58, v228
	v_med3_f32 v17, v105, s58, v228
	v_cvt_pk_fp8_f32 v242, v14, v15
	s_nop 0
	v_cvt_pk_fp8_f32 v242, v16, v17 op_sel:[0,0,1]
	v_med3_f32 v14, v94, s58, v228
	v_med3_f32 v15, v95, s58, v228
	v_med3_f32 v16, v96, s58, v228
	v_med3_f32 v17, v97, s58, v228
	v_cvt_pk_fp8_f32 v243, v14, v15
	s_nop 0
	v_cvt_pk_fp8_f32 v243, v16, v17 op_sel:[0,0,1]
	v_med3_f32 v14, v98, s58, v228
	v_med3_f32 v15, v99, s58, v228
	v_med3_f32 v16, v100, s58, v228
	v_med3_f32 v17, v101, s58, v228
	v_cvt_pk_fp8_f32 v244, v14, v15
	s_nop 0
	v_cvt_pk_fp8_f32 v244, v16, v17 op_sel:[0,0,1]
	v_med3_f32 v14, v90, s58, v228
	v_med3_f32 v15, v91, s58, v228
	v_med3_f32 v16, v92, s58, v228
	v_med3_f32 v17, v93, s58, v228
	v_cvt_pk_fp8_f32 v245, v14, v15
	s_nop 0
	v_cvt_pk_fp8_f32 v245, v16, v17 op_sel:[0,0,1]
	v_med3_f32 v14, v86, s58, v228
	v_med3_f32 v15, v87, s58, v228
	v_med3_f32 v16, v88, s58, v228
	v_med3_f32 v17, v89, s58, v228
	v_cvt_pk_fp8_f32 v246, v14, v15
	s_nop 0
	v_cvt_pk_fp8_f32 v246, v16, v17 op_sel:[0,0,1]
	v_med3_f32 v14, v78, s58, v228
	v_med3_f32 v15, v79, s58, v228
	v_med3_f32 v16, v80, s58, v228
	v_med3_f32 v17, v81, s58, v228
	v_cvt_pk_fp8_f32 v247, v14, v15
	s_nop 0
	v_cvt_pk_fp8_f32 v247, v16, v17 op_sel:[0,0,1]
	v_med3_f32 v14, v82, s58, v228
	v_med3_f32 v15, v83, s58, v228
	v_med3_f32 v16, v84, s58, v228
	v_med3_f32 v17, v85, s58, v228
	v_cvt_pk_fp8_f32 v248, v14, v15
	s_nop 0
	v_cvt_pk_fp8_f32 v248, v16, v17 op_sel:[0,0,1]
	v_med3_f32 v14, v74, s58, v228
	v_med3_f32 v15, v75, s58, v228
	v_med3_f32 v16, v76, s58, v228
	v_med3_f32 v17, v77, s58, v228
	v_cvt_pk_fp8_f32 v249, v14, v15
	s_nop 0
	v_cvt_pk_fp8_f32 v249, v16, v17 op_sel:[0,0,1]
	v_med3_f32 v14, v70, s58, v228
	v_med3_f32 v15, v71, s58, v228
	v_med3_f32 v16, v72, s58, v228
	v_med3_f32 v17, v73, s58, v228
	v_cvt_pk_fp8_f32 v250, v14, v15
	s_nop 0
	v_cvt_pk_fp8_f32 v250, v16, v17 op_sel:[0,0,1]
	v_med3_f32 v14, v66, s58, v228
	v_med3_f32 v15, v67, s58, v228
	v_med3_f32 v16, v68, s58, v228
	v_med3_f32 v17, v69, s58, v228
	v_cvt_pk_fp8_f32 v251, v14, v15
	s_nop 0
	v_cvt_pk_fp8_f32 v251, v16, v17 op_sel:[0,0,1]
	s_mov_b32 s98, s64
	s_lshl_b32 s99, s20, 8
	s_andn2_b64 vcc, exec, s[18:19]
	s_mov_b64 s[18:19], -1
	s_cbranch_vccnz .LBB0_938
	s_andn2_b64 vcc, exec, s[6:7]
	s_cbranch_vccnz .LBB0_937
	s_barrier
	s_branch .LBB0_937
.LBB0_953:
	v_add_u32_e32 v252, s98, v221
	v_lshlrev_b32_e32 v252, 11, v252
	v_add3_u32 v252, v252, s99, v223
	v_add_u32_e32 v252, 0x48000, v252
	global_store_dwordx4 v252, v[240:243], s[8:9]
	s_nop 1
	v_add_u32_e32 v252, s98, v221
	v_lshlrev_b32_e32 v252, 11, v252
	v_add3_u32 v252, v252, s99, v223
	v_add_u32_e32 v252, 0x50000, v252
	global_store_dwordx4 v252, v[244:247], s[8:9]
	s_nop 1
	v_add_u32_e32 v252, s98, v221
	v_lshlrev_b32_e32 v252, 11, v252
	v_add3_u32 v252, v252, s99, v223
	v_add_u32_e32 v252, 0x58000, v252
	global_store_dwordx4 v252, v[248:251], s[8:9]
	s_nop 1
	s_waitcnt vmcnt(0)
	s_barrier

; __global__ void __launch_bounds__(NWAVES * 64, 2) fwd_kernel(Args args) {
	.amdhsa_kernel _Z10fwd_kernel4Args
		.amdhsa_group_segment_fixed_size 0
		.amdhsa_private_segment_fixed_size 0
		.amdhsa_kernarg_size 480
		.amdhsa_user_sgpr_count 2
		.amdhsa_user_sgpr_dispatch_ptr 0
		.amdhsa_user_sgpr_queue_ptr 0
		.amdhsa_user_sgpr_kernarg_segment_ptr 1
		.amdhsa_user_sgpr_dispatch_id 0
		.amdhsa_user_sgpr_kernarg_preload_length 0
		.amdhsa_user_sgpr_kernarg_preload_offset 0
		.amdhsa_user_sgpr_private_segment_size 0
		.amdhsa_uses_dynamic_stack 0
		.amdhsa_enable_private_segment 0
		.amdhsa_system_sgpr_workgroup_id_x 1
		.amdhsa_system_sgpr_workgroup_id_y 0
		.amdhsa_system_sgpr_workgroup_id_z 0
		.amdhsa_system_sgpr_workgroup_info 0
		.amdhsa_system_vgpr_workitem_id 0
		.amdhsa_next_free_vgpr 256
		.amdhsa_next_free_sgpr 102
		.amdhsa_accum_offset 256
		.amdhsa_reserve_vcc 1
		.amdhsa_float_round_mode_32 0
		.amdhsa_float_round_mode_16_64 0
		.amdhsa_float_denorm_mode_32 3
		.amdhsa_float_denorm_mode_16_64 3
		.amdhsa_dx10_clamp 1
		.amdhsa_ieee_mode 1
		.amdhsa_fp16_overflow 0
		.amdhsa_tg_split 0
		.amdhsa_exception_fp_ieee_invalid_op 0
		.amdhsa_exception_fp_denorm_src 0
		.amdhsa_exception_fp_ieee_div_zero 0
		.amdhsa_exception_fp_ieee_overflow 0
		.amdhsa_exception_fp_ieee_underflow 0
		.amdhsa_exception_fp_ieee_inexact 0
		.amdhsa_exception_int_div_zero 0
	.end_amdhsa_kernel

; __global__ void __launch_bounds__(NWAVES * 64, 2) fwd_kernel(Args args) {
amdhsa.kernels:
  - .agpr_count:     0
    .args:
      - .offset:         0
        .size:           224
        .value_kind:     by_value
      - .offset:         224
        .size:           4
        .value_kind:     hidden_block_count_x
      - .offset:         228
        .size:           4
        .value_kind:     hidden_block_count_y
      - .offset:         232
        .size:           4
        .value_kind:     hidden_block_count_z
      - .offset:         236
        .size:           2
        .value_kind:     hidden_group_size_x
      - .offset:         238
        .size:           2
        .value_kind:     hidden_group_size_y
      - .offset:         240
        .size:           2
        .value_kind:     hidden_group_size_z
      - .offset:         242
        .size:           2
        .value_kind:     hidden_remainder_x
      - .offset:         244
        .size:           2
        .value_kind:     hidden_remainder_y
      - .offset:         246
        .size:           2
        .value_kind:     hidden_remainder_z
      - .offset:         264
        .size:           8
        .value_kind:     hidden_global_offset_x
      - .offset:         272
        .size:           8
        .value_kind:     hidden_global_offset_y
      - .offset:         280
        .size:           8
        .value_kind:     hidden_global_offset_z
      - .offset:         288
        .size:           2
        .value_kind:     hidden_grid_dims
      - .offset:         344
        .size:           4
        .value_kind:     hidden_dynamic_lds_size
    .group_segment_fixed_size: 0
    .kernarg_segment_align: 8
    .kernarg_segment_size: 480
    .language:       OpenCL C
    .language_version:
      - 2
      - 0
    .max_flat_workgroup_size: 512
    .name:           _Z10fwd_kernel4Args
    .private_segment_fixed_size: 0
    .sgpr_count:     108
    .sgpr_spill_count: 234
    .symbol:         _Z10fwd_kernel4Args.kd
    .uniform_work_group_size: 1
    .uses_dynamic_stack: false
    .vgpr_count:     256
    .vgpr_spill_count: 0
    .wavefront_size: 64
